# priority: S3 static wave-half raise removed as well (no s_setprio anywhere), on top of v52
# baseline (speedup 1.0000x reference)
.LBB0_693:
	s_or_b64 exec, exec, s[4:5]
	s_mov_b32 s0, s86
	s_waitcnt lgkmcnt(0)
	s_waitcnt vmcnt(0)
	s_barrier
	v_mbcnt_lo_u32_b32 v0, -1, 0
	v_mbcnt_hi_u32_b32 v0, -1, v0
	s_mov_b32 s60, s79
	v_lshl_add_u32 v0, s0, 6, v0
	s_mov_b32 s0, s79
	s_add_i32 s0, s0, 0x25f98
	v_mov_b32_e32 v1, s0
	ds_read_b64 v[2:3], v1
	s_mov_b32 s2, s79
	s_add_i32 s2, s2, 0x25f60
	v_mov_b32_e32 v1, s2
	s_waitcnt lgkmcnt(0)
	v_readfirstlane_b32 s0, v2
	v_readfirstlane_b32 s1, v3
	ds_read_b64 v[2:3], v1
	s_mov_b32 s4, s79
	s_add_i32 s4, s4, 0x25f58
	v_mov_b32_e32 v1, s4
	s_waitcnt lgkmcnt(0)
	v_readfirstlane_b32 s2, v2
	v_readfirstlane_b32 s3, v3
	ds_read_b64 v[2:3], v1
	v_readfirstlane_b32 s70, v0
	s_ashr_i32 s18, s70, 6
	s_cmp_gt_i32 s18, 3
	s_cselect_b64 s[4:5], -1, 0
	s_waitcnt lgkmcnt(0)
	v_readfirstlane_b32 s6, v2
	v_readfirstlane_b32 s7, v3
	s_cmp_lt_i32 s18, 4
	s_cbranch_scc1 .LBB0_695
.LBB0_695:
	v_readlane_b32 s8, v242, 4
	v_readlane_b32 s9, v242, 5
	s_andn2_b64 vcc, exec, s[8:9]
	s_cbranch_vccnz .LBB0_753
	s_add_u32 s10, s0, 0x43800000
	s_addc_u32 s11, s1, 0
	s_add_u32 s8, s0, 0x69900000
	s_addc_u32 s9, s1, 0
	v_writelane_b32 v242, s8, 60
	v_bfe_u32 v2, v0, 4, 2
	v_lshlrev_b32_e32 v1, 2, v0
	v_writelane_b32 v242, s9, 61
	s_add_u32 s8, s0, 0x3f700000
	v_writelane_b32 v241, s8, 0
	s_addc_u32 s8, s1, 0
	v_writelane_b32 v241, s8, 2
	v_readlane_b32 s8, v243, 47
	v_readlane_b32 s9, v243, 48
	s_add_u32 s0, s0, s8
	s_addc_u32 s1, s1, s9
	s_add_u32 s28, s0, 0x6dc00000
	s_addc_u32 s29, s1, 0
	v_readlane_b32 s0, v241, 4
	v_readlane_b32 s1, v241, 5
	s_add_u32 s0, s2, s0
	v_writelane_b32 v241, s0, 59
	s_addc_u32 s0, s3, s1
	v_writelane_b32 v241, s0, 61
	v_and_b32_e32 v1, 60, v1
	v_readlane_b32 s0, v241, 8
	v_readlane_b32 s1, v241, 9
	s_add_u32 s20, s6, s0
	s_addc_u32 s21, s7, s1
	s_lshl_b32 s0, s18, 1
	s_and_b32 s0, s0, 0x3ffffc
	v_or_b32_e32 v2, s0, v2
	s_lshl_b32 s69, s18, 5
	s_lshl_b32 s1, s18, 3
	v_writelane_b32 v241, s10, 14
	v_lshlrev_b32_e32 v2, 10, v2
	s_and_b32 s0, s69, 32
	v_writelane_b32 v241, s11, 15
	v_bitop3_b32 v1, v2, s0, v1 bitop3:0xf6
	s_sub_i32 s0, 63, s1
	s_lshl_b32 s7, s18, 9
	v_writelane_b32 v241, s0, 19
	v_cvt_f32_i32_e32 v147, s0
	s_and_b32 s0, s7, 0x200
	v_or_b32_e32 v148, s0, v1
	s_or_b32 s0, s1, 1
	s_sub_i32 s2, 63, s0
	v_writelane_b32 v241, s2, 21
	v_writelane_b32 v241, s0, 23
	s_lshl_b32 s0, s0, 6
	s_and_b32 s0, s0, 0x240
	v_or_b32_e32 v2, s0, v1
	s_or_b32 s0, s1, 2
	v_cvt_f32_i32_e32 v149, s2
	s_sub_i32 s2, 63, s0
	v_writelane_b32 v241, s2, 25
	v_writelane_b32 v241, s0, 27
	s_lshl_b32 s0, s0, 6
	s_and_b32 s0, s0, 0x280
	v_or_b32_e32 v3, s0, v1
	s_or_b32 s0, s1, 3
	v_cvt_f32_i32_e32 v150, s2
	s_sub_i32 s2, 63, s0
	v_writelane_b32 v241, s2, 29
	v_writelane_b32 v241, s0, 31
	s_lshl_b32 s0, s0, 6
	s_and_b32 s0, s0, 0x2c0
	s_waitcnt vmcnt(8)
	v_or_b32_e32 v4, s0, v1
	s_or_b32 s0, s1, 4
	v_cvt_f32_i32_e32 v151, s2
	s_sub_i32 s2, 63, s0
	v_writelane_b32 v241, s2, 33
	v_writelane_b32 v241, s0, 35
	s_lshl_b32 s0, s0, 6
	s_and_b32 s0, s0, 0x300
	v_or_b32_e32 v5, s0, v1
	s_or_b32 s0, s1, 5
	v_cvt_f32_i32_e32 v152, s2
	s_sub_i32 s2, 63, s0
	v_writelane_b32 v241, s2, 37
	v_writelane_b32 v241, s0, 39
	s_lshl_b32 s0, s0, 6
	s_and_b32 s0, s0, 0x340
	v_or_b32_e32 v6, s0, v1
	s_or_b32 s0, s1, 6
	v_cvt_f32_i32_e32 v153, s2
	s_sub_i32 s2, 63, s0
	v_writelane_b32 v241, s2, 41
	v_writelane_b32 v241, s0, 43
	s_lshl_b32 s0, s0, 6
	s_and_b32 s0, s0, 0x380
	v_or_b32_e32 v7, s0, v1
	s_or_b32 s0, s1, 7
	v_writelane_b32 v241, s1, 45
	s_sub_i32 s1, 63, s0
	v_writelane_b32 v241, s1, 47
	v_writelane_b32 v241, s0, 49
	s_lshl_b32 s0, s0, 6
	s_and_b32 s0, s0, 0x3c0
	v_or_b32_e32 v8, s0, v1
	v_lshrrev_b32_e32 v1, 2, v0
	s_ashr_i32 s66, s70, 8
	v_and_b32_e32 v1, 14, v1
	v_lshlrev_b32_e32 v9, 7, v0
	v_and_b32_e32 v146, 63, v0
	v_add_lshl_u32 v1, v1, s66, 10
	v_and_b32_e32 v9, 0x380, v9
	v_lshlrev_b32_e32 v64, 2, v146
	v_add3_u32 v158, s60, v1, v9
	v_ashrrev_i32_e32 v1, 31, v0
	v_lshl_add_u64 v[66:67], s[10:11], 0, v[64:65]
	v_lshlrev_b64 v[68:69], 3, v[0:1]
	s_mov_b64 s[10:11], 0x1000
	v_lshl_add_u64 v[70:71], v[68:69], 0, s[10:11]
	s_mov_b64 s[10:11], 0x2000
	s_bfe_u32 s6, s70, 0x20006
	v_lshl_add_u64 v[72:73], v[68:69], 0, s[10:11]
	s_mov_b64 s[10:11], 0x3000
	v_cvt_f32_i32_e32 v155, s1
	s_lshl_b32 s1, s6, 12
	v_lshl_add_u64 v[74:75], v[68:69], 0, s[10:11]
	s_mov_b64 s[10:11], 0x4000
	v_cvt_f32_i32_e32 v154, s2
	s_and_b32 s0, s18, -4
	s_add_i32 s2, s60, s1
	s_lshl_b32 s1, s6, 11
	v_lshl_add_u64 v[76:77], v[68:69], 0, s[10:11]
	s_mov_b64 s[10:11], 0x5000
	v_lshlrev_b32_e32 v156, 3, v146
	s_add_i32 s64, s60, 0x12000
	s_add_i32 s3, s60, s1
	s_lshl_b32 s1, s0, 12
	v_lshl_add_u64 v[78:79], v[68:69], 0, s[10:11]
	s_mov_b64 s[10:11], 0x6000
	s_lshl_b32 s8, s18, 4
	v_and_b32_e32 v10, 32, v156
	s_add_i32 s97, s64, s1
	s_lshl_b32 s1, s0, 11
	v_lshl_add_u64 v[80:81], v[68:69], 0, s[10:11]
	s_mov_b64 s[10:11], 0x7000
	v_bitop3_b32 v157, s8, v10, 48 bitop3:0x6c
	s_add_i32 s61, s60, s1
	s_lshl_b32 s1, s18, 11
	s_lshl_b32 s25, s66, 6
	v_lshl_add_u64 v[82:83], v[68:69], 0, s[10:11]
	s_lshl_b32 s0, s0, 4
	s_or_b32 s22, s8, 48
	s_lshl_b32 s8, s6, 8
	s_lshl_b32 s10, s66, 7
	s_lshl_b32 s68, s6, 4
	s_lshl_b32 s9, s66, 1
	s_add_i32 s3, s3, 0x10000
	s_add_i32 s62, s60, s1
	s_add_i32 s24, s60, 0x1b600
	s_xor_b32 s82, s25, 64
	s_lshl_b32 s42, s6, 1
	s_ashr_i32 s1, s0, 31
	s_ashr_i32 s23, s22, 31
	s_add_i32 s8, s8, s10
	s_cmp_le_i32 s9, s6
	v_writelane_b32 v241, s8, 51
	s_cselect_b64 s[30:31], -1, 0
	s_lshl_b32 s86, s66, 13
	s_lshl_b32 s87, s66, 5
	s_lshl_b32 s63, s66, 10
	s_or_b32 s8, s9, 1
	s_cmp_lt_i32 s9, s6
	s_cselect_b64 s[34:35], -1, 0
	s_add_i32 s26, s60, 0x1a000
	s_lshl_b32 s65, s8, 12
	s_lshl_b32 s90, s8, 4
	s_lshl_b32 s91, s8, 5
	s_add_i32 s80, s26, s7
	s_cmp_gt_i32 s18, 0
	s_cselect_b64 s[6:7], -1, 0
	s_cmp_gt_i32 s18, 1
	s_cselect_b64 s[8:9], -1, 0
	s_cmp_gt_i32 s18, 2
	s_cselect_b64 s[10:11], -1, 0
	s_cmp_gt_i32 s18, 4
	s_cselect_b64 s[12:13], -1, 0
	s_cmp_gt_i32 s18, 5
	s_cselect_b64 s[14:15], -1, 0
	s_cmp_gt_i32 s18, 6
	s_cselect_b64 s[16:17], -1, 0
	s_cmp_gt_i32 s18, 7
	s_cselect_b64 s[18:19], -1, 0
	s_cmp_lt_u32 s70, 64
	s_cselect_b64 s[36:37], -1, 0
	s_add_i32 s27, s60, 0x1b000
	s_add_i32 s33, s60, 0x1b200
	s_add_i32 s67, s60, 0x1b400
	s_andn2_b32 s70, s70, 63
	s_lshl_b64 s[38:39], s[0:1], 2
	s_add_u32 s38, s20, s38
	s_addc_u32 s39, s21, s39
	s_lshl_b64 s[40:41], s[22:23], 2
	s_add_u32 s40, s20, s40
	s_addc_u32 s41, s21, s41
	s_or_b32 s20, s42, 56
	v_add_u32_e32 v159, s60, v2
	v_add_u32_e32 v160, s60, v3
	v_add_u32_e32 v161, s60, v4
	v_add_u32_e32 v162, s60, v5
	v_add_u32_e32 v163, s60, v6
	v_add_u32_e32 v164, s60, v7
	v_add_u32_e32 v165, s60, v8
	s_mov_b32 s43, s74
	v_writelane_b32 v241, s20, 53
	s_branch .LBB0_699

.LBB0_752:
	v_readlane_b32 s74, v242, 38
	v_readlane_b32 s75, v242, 39
	v_readlane_b32 s76, v242, 42
	v_readlane_b32 s82, v242, 45
	v_readlane_b32 s90, v242, 49
	v_readlane_b32 s88, v241, 12
	v_readlane_b32 s71, v242, 41
	v_readlane_b32 s77, v242, 43
	v_readlane_b32 s80, v242, 44
	v_readlane_b32 s83, v242, 46
	v_readlane_b32 s84, v242, 47
	v_readlane_b32 s86, v242, 48
	v_readlane_b32 s91, v242, 50
	s_movk_i32 s87, 0x100
	s_mov_b64 s[68:69], 0x80
	v_readlane_b32 s89, v241, 13
	v_readlane_b32 s75, v241, 16
.LBB0_753:
	s_mov_b32 s2, s84
	s_waitcnt vmcnt(0)
	s_barrier
	v_readlane_b32 s100, v242, 48
	s_nop 3
	s_cmp_lg_u32 s100, 1
	s_cbranch_scc1 .Lxb_skipinv_6
	buffer_inv sc1
